# best2 with the final combine's output stores back at the default cache policy (nt kept on its loads)
# speedup vs baseline: 1.0124x; 1.0124x over previous
; DI void p11_combine(Frame& F) {
;     ...
;     for (int tok = gw; tok < NTOK; tok += NGW) {
;         const int tn = tok + NGW < NTOK ? tok + NGW : tok;
;         const int4 psn = *(const int4*)(POS + (size_t)tn * 4);
;         f32x4* orow = (f32x4*)(F.out + (size_t)tok * DM) + F.lane;
;         const unsigned* y0 = (const unsigned*)(YB + (size_t)ps.x * DM) + F.lane; const unsigned* y1 = (const unsigned*)(YB + (size_t)ps.y * DM) + F.lane;
;         const unsigned* y2 = (const unsigned*)(YB + (size_t)ps.z * DM) + F.lane; const unsigned* y3 = (const unsigned*)(YB + (size_t)ps.w * DM) + F.lane;
;         f32x4 v[8]; unsigned qa[8], qb[8], qc[8], qd[8];
; #pragma unroll
;         for (int j = 0; j < 8; ++j) { v[j] = orow[64 * j]; qa[j] = y0[64 * j]; qb[j] = y1[64 * j]; qc[j] = y2[64 * j]; qd[j] = y3[64 * j]; }
;         __builtin_amdgcn_sched_barrier(0);
; #pragma unroll
;         for (int j = 0; j < 8; ++j) { const unsigned a = qa[j], bq = qb[j], cq = qc[j], dq = qd[j];
;             const f32x2 a0 = __builtin_amdgcn_cvt_pk_f32_fp8((int)a, false), a1 = __builtin_amdgcn_cvt_pk_f32_fp8((int)a, true), b0 = __builtin_amdgcn_cvt_pk_f32_fp8((int)bq, false), b1 = __builtin_amdgcn_cvt_pk_f32_fp8((int)bq, true);
;             const f32x2 c0 = __builtin_amdgcn_cvt_pk_f32_fp8((int)cq, false), c1 = __builtin_amdgcn_cvt_pk_f32_fp8((int)cq, true), d0 = __builtin_amdgcn_cvt_pk_f32_fp8((int)dq, false), d1 = __builtin_amdgcn_cvt_pk_f32_fp8((int)dq, true);
.LBB0_1225:
	s_add_i32 s5, s10, s4
	s_cmp_lt_i32 s5, 0x8000
	s_cselect_b64 s[14:15], -1, 0
	s_and_b64 vcc, s[14:15], exec
	s_cselect_b32 s10, s5, s10
	s_ashr_i32 s11, s10, 31
	s_lshl_b64 s[10:11], s[10:11], 4
	s_add_u32 s10, s9, s10
	s_addc_u32 s11, s12, s11
	global_load_dwordx4 v[38:41], v33, s[10:11]
	s_ashr_i32 s11, s0, 31
	s_mov_b32 s10, s0
	s_lshl_b64 s[10:11], s[10:11], 11
	v_lshl_add_u64 v[42:43], v[34:35], 0, s[10:11]
	s_ashr_i32 s11, s1, 31
	s_mov_b32 s10, s1
	s_lshl_b64 s[0:1], s[10:11], 11
	v_lshl_add_u64 v[44:45], v[34:35], 0, s[0:1]
	s_ashr_i32 s1, s2, 31
	s_mov_b32 s0, s2
	s_lshl_b64 s[0:1], s[0:1], 11
	v_lshl_add_u64 v[46:47], v[34:35], 0, s[0:1]
	s_ashr_i32 s1, s3, 31
	s_mov_b32 s0, s3
	s_lshl_b64 s[0:1], s[0:1], 11
	v_lshl_add_u64 v[48:49], v[34:35], 0, s[0:1]
	global_load_dwordx4 v[0:3], v[36:37], off offset:-4096 nt
	global_load_dwordx4 v[4:7], v[36:37], off offset:-3072 nt
	s_waitcnt lgkmcnt(0)
	global_load_dwordx4 v[8:11], v[36:37], off offset:-2048 nt
	global_load_dwordx4 v[12:15], v[36:37], off offset:-1024 nt
	global_load_dwordx4 v[16:19], v[36:37], off nt
	global_load_dwordx4 v[20:23], v[36:37], off offset:1024 nt
	global_load_dwordx4 v[24:27], v[36:37], off offset:2048 nt
	global_load_dwordx4 v[28:31], v[36:37], off offset:3072 nt
	global_load_dword v32, v[42:43], off nt
	global_load_dword v56, v[42:43], off offset:256 nt
	global_load_dword v72, v[42:43], off offset:512 nt
	global_load_dword v88, v[42:43], off offset:768 nt
	global_load_dword v104, v[42:43], off offset:1024 nt
	global_load_dword v120, v[42:43], off offset:1280 nt
	global_load_dword v136, v[42:43], off offset:1536 nt
	global_load_dword v152, v[42:43], off offset:1792 nt
	global_load_dword v50, v[44:45], off nt
	global_load_dword v60, v[44:45], off offset:256 nt
	global_load_dword v76, v[44:45], off offset:512 nt
	global_load_dword v92, v[44:45], off offset:768 nt
	global_load_dword v108, v[44:45], off offset:1024 nt
	global_load_dword v124, v[44:45], off offset:1280 nt
	global_load_dword v140, v[44:45], off offset:1536 nt
	global_load_dword v156, v[44:45], off offset:1792 nt
	global_load_dword v51, v[46:47], off nt
	global_load_dword v64, v[46:47], off offset:256 nt
	global_load_dword v80, v[46:47], off offset:512 nt
	global_load_dword v96, v[46:47], off offset:768 nt
	global_load_dword v112, v[46:47], off offset:1024 nt
	global_load_dword v128, v[46:47], off offset:1280 nt
	global_load_dword v144, v[46:47], off offset:1536 nt
	global_load_dword v160, v[46:47], off offset:1792 nt
	global_load_dword v52, v[48:49], off nt
	global_load_dword v68, v[48:49], off offset:256 nt
	global_load_dword v84, v[48:49], off offset:512 nt
	global_load_dword v100, v[48:49], off offset:768 nt
	global_load_dword v116, v[48:49], off offset:1024 nt
	global_load_dword v132, v[48:49], off offset:1280 nt
	global_load_dword v148, v[48:49], off offset:1536 nt
	global_load_dword v164, v[48:49], off offset:1792 nt
	s_waitcnt vmcnt(40)
	v_readfirstlane_b32 s0, v38
	v_readfirstlane_b32 s1, v39
	v_readfirstlane_b32 s2, v40
	v_readfirstlane_b32 s3, v41
	s_waitcnt vmcnt(31)
	v_cvt_pk_f32_fp8_e32 v[38:39], v32
	v_cvt_pk_f32_fp8_sdwa v[40:41], v32 src0_sel:WORD_1
	s_waitcnt vmcnt(23)
	v_cvt_pk_f32_fp8_e32 v[42:43], v50
	v_cvt_pk_f32_fp8_sdwa v[44:45], v50 src0_sel:WORD_1
	s_waitcnt vmcnt(15)
	v_cvt_pk_f32_fp8_e32 v[46:47], v51
	v_cvt_pk_f32_fp8_sdwa v[48:49], v51 src0_sel:WORD_1
	v_cvt_pk_f32_fp8_e32 v[54:55], v56
	v_cvt_pk_f32_fp8_sdwa v[56:57], v56 src0_sel:WORD_1
	v_cvt_pk_f32_fp8_e32 v[58:59], v60
	v_cvt_pk_f32_fp8_sdwa v[60:61], v60 src0_sel:WORD_1
	v_cvt_pk_f32_fp8_e32 v[70:71], v72
	v_cvt_pk_f32_fp8_sdwa v[72:73], v72 src0_sel:WORD_1
	v_cvt_pk_f32_fp8_e32 v[74:75], v76
	v_cvt_pk_f32_fp8_sdwa v[76:77], v76 src0_sel:WORD_1
	v_cvt_pk_f32_fp8_e32 v[86:87], v88
	v_cvt_pk_f32_fp8_sdwa v[88:89], v88 src0_sel:WORD_1
	v_cvt_pk_f32_fp8_e32 v[90:91], v92
	v_cvt_pk_f32_fp8_sdwa v[92:93], v92 src0_sel:WORD_1
	v_cvt_pk_f32_fp8_e32 v[102:103], v104
	v_cvt_pk_f32_fp8_sdwa v[104:105], v104 src0_sel:WORD_1
	v_cvt_pk_f32_fp8_e32 v[106:107], v108
	v_cvt_pk_f32_fp8_sdwa v[108:109], v108 src0_sel:WORD_1
	v_cvt_pk_f32_fp8_e32 v[118:119], v120
	v_cvt_pk_f32_fp8_sdwa v[120:121], v120 src0_sel:WORD_1
	v_cvt_pk_f32_fp8_e32 v[122:123], v124
	v_cvt_pk_f32_fp8_sdwa v[124:125], v124 src0_sel:WORD_1
	v_cvt_pk_f32_fp8_e32 v[134:135], v136
	v_cvt_pk_f32_fp8_sdwa v[136:137], v136 src0_sel:WORD_1
	v_cvt_pk_f32_fp8_e32 v[138:139], v140
	v_cvt_pk_f32_fp8_sdwa v[140:141], v140 src0_sel:WORD_1
	v_cvt_pk_f32_fp8_e32 v[150:151], v152
	v_cvt_pk_f32_fp8_sdwa v[152:153], v152 src0_sel:WORD_1
	v_cvt_pk_f32_fp8_e32 v[154:155], v156
	v_cvt_pk_f32_fp8_sdwa v[156:157], v156 src0_sel:WORD_1
	s_waitcnt vmcnt(7)
; DI void p11_combine(Frame& F) {
;     ...
;         for (int j = 0; j < 8; ++j) { const unsigned a = qa[j], bq = qb[j], cq = qc[j], dq = qd[j];
;             const f32x2 a0 = __builtin_amdgcn_cvt_pk_f32_fp8((int)a, false), a1 = __builtin_amdgcn_cvt_pk_f32_fp8((int)a, true), b0 = __builtin_amdgcn_cvt_pk_f32_fp8((int)bq, false), b1 = __builtin_amdgcn_cvt_pk_f32_fp8((int)bq, true);
;             const f32x2 c0 = __builtin_amdgcn_cvt_pk_f32_fp8((int)cq, false), c1 = __builtin_amdgcn_cvt_pk_f32_fp8((int)cq, true), d0 = __builtin_amdgcn_cvt_pk_f32_fp8((int)dq, false), d1 = __builtin_amdgcn_cvt_pk_f32_fp8((int)dq, true);
;             f32x4 vv = v[j];
;             vv[0] += (((a0[0] + b0[0]) + c0[0]) + d0[0]) * 0.0625f; vv[1] += (((a0[1] + b0[1]) + c0[1]) + d0[1]) * 0.0625f;
;             vv[2] += (((a1[0] + b1[0]) + c1[0]) + d1[0]) * 0.0625f; vv[3] += (((a1[1] + b1[1]) + c1[1]) + d1[1]) * 0.0625f; orow[64 * j] = vv; }
;         ps = psn;
	v_cvt_pk_f32_fp8_e32 v[50:51], v52
	v_cvt_pk_f32_fp8_sdwa v[52:53], v52 src0_sel:WORD_1
	v_cvt_pk_f32_fp8_e32 v[62:63], v64
	v_cvt_pk_f32_fp8_sdwa v[64:65], v64 src0_sel:WORD_1
	v_cvt_pk_f32_fp8_e32 v[78:79], v80
	v_cvt_pk_f32_fp8_sdwa v[80:81], v80 src0_sel:WORD_1
	v_cvt_pk_f32_fp8_e32 v[94:95], v96
	v_cvt_pk_f32_fp8_sdwa v[96:97], v96 src0_sel:WORD_1
	v_cvt_pk_f32_fp8_e32 v[110:111], v112
	v_cvt_pk_f32_fp8_sdwa v[112:113], v112 src0_sel:WORD_1
	v_cvt_pk_f32_fp8_e32 v[126:127], v128
	v_cvt_pk_f32_fp8_sdwa v[128:129], v128 src0_sel:WORD_1
	v_cvt_pk_f32_fp8_e32 v[142:143], v144
	v_cvt_pk_f32_fp8_sdwa v[144:145], v144 src0_sel:WORD_1
	v_cvt_pk_f32_fp8_e32 v[158:159], v160
	v_cvt_pk_f32_fp8_sdwa v[160:161], v160 src0_sel:WORD_1
	s_waitcnt vmcnt(6)
	v_cvt_pk_f32_fp8_e32 v[66:67], v68
	v_cvt_pk_f32_fp8_sdwa v[68:69], v68 src0_sel:WORD_1
	s_waitcnt vmcnt(5)
	v_cvt_pk_f32_fp8_e32 v[82:83], v84
	v_cvt_pk_f32_fp8_sdwa v[84:85], v84 src0_sel:WORD_1
	s_waitcnt vmcnt(4)
	v_cvt_pk_f32_fp8_e32 v[98:99], v100
	v_cvt_pk_f32_fp8_sdwa v[100:101], v100 src0_sel:WORD_1
	s_waitcnt vmcnt(3)
	v_cvt_pk_f32_fp8_e32 v[114:115], v116
	v_cvt_pk_f32_fp8_sdwa v[116:117], v116 src0_sel:WORD_1
	s_waitcnt vmcnt(2)
	v_cvt_pk_f32_fp8_e32 v[130:131], v132
	v_cvt_pk_f32_fp8_sdwa v[132:133], v132 src0_sel:WORD_1
	s_waitcnt vmcnt(1)
	v_cvt_pk_f32_fp8_e32 v[146:147], v148
	v_cvt_pk_f32_fp8_sdwa v[148:149], v148 src0_sel:WORD_1
	s_waitcnt vmcnt(0)
	v_cvt_pk_f32_fp8_e32 v[162:163], v164
	v_cvt_pk_f32_fp8_sdwa v[164:165], v164 src0_sel:WORD_1
	v_pk_add_f32 v[38:39], v[38:39], v[42:43]
	v_pk_add_f32 v[40:41], v[40:41], v[44:45]
	v_pk_add_f32 v[42:43], v[54:55], v[58:59]
	v_pk_add_f32 v[44:45], v[56:57], v[60:61]
	v_pk_add_f32 v[54:55], v[70:71], v[74:75]
	v_pk_add_f32 v[56:57], v[72:73], v[76:77]
	v_pk_add_f32 v[58:59], v[86:87], v[90:91]
	v_pk_add_f32 v[60:61], v[88:89], v[92:93]
	v_pk_add_f32 v[70:71], v[102:103], v[106:107]
	v_pk_add_f32 v[72:73], v[104:105], v[108:109]
	v_pk_add_f32 v[74:75], v[118:119], v[122:123]
	v_pk_add_f32 v[76:77], v[120:121], v[124:125]
	v_pk_add_f32 v[86:87], v[134:135], v[138:139]
	v_pk_add_f32 v[88:89], v[136:137], v[140:141]
	v_pk_add_f32 v[90:91], v[150:151], v[154:155]
	v_pk_add_f32 v[92:93], v[152:153], v[156:157]
	v_pk_add_f32 v[38:39], v[38:39], v[46:47]
	v_pk_add_f32 v[40:41], v[40:41], v[48:49]
	v_pk_add_f32 v[42:43], v[42:43], v[62:63]
	v_pk_add_f32 v[44:45], v[44:45], v[64:65]
	v_pk_add_f32 v[46:47], v[54:55], v[78:79]
	v_pk_add_f32 v[48:49], v[56:57], v[80:81]
	v_pk_add_f32 v[54:55], v[58:59], v[94:95]
	v_pk_add_f32 v[56:57], v[60:61], v[96:97]
	v_pk_add_f32 v[58:59], v[70:71], v[110:111]
	v_pk_add_f32 v[60:61], v[72:73], v[112:113]
	v_pk_add_f32 v[62:63], v[74:75], v[126:127]
	v_pk_add_f32 v[64:65], v[76:77], v[128:129]
	v_pk_add_f32 v[70:71], v[86:87], v[142:143]
	v_pk_add_f32 v[72:73], v[88:89], v[144:145]
	v_pk_add_f32 v[74:75], v[90:91], v[158:159]
	v_pk_add_f32 v[76:77], v[92:93], v[160:161]
	v_pk_add_f32 v[38:39], v[38:39], v[50:51]
	v_pk_add_f32 v[40:41], v[40:41], v[52:53]
	v_pk_add_f32 v[42:43], v[42:43], v[66:67]
	v_pk_add_f32 v[44:45], v[44:45], v[68:69]
	v_pk_add_f32 v[46:47], v[46:47], v[82:83]
	v_pk_add_f32 v[48:49], v[48:49], v[84:85]
	v_pk_add_f32 v[50:51], v[54:55], v[98:99]
	v_pk_add_f32 v[52:53], v[56:57], v[100:101]
	v_pk_add_f32 v[54:55], v[58:59], v[114:115]
	v_pk_add_f32 v[56:57], v[60:61], v[116:117]
	v_pk_add_f32 v[58:59], v[62:63], v[130:131]
	v_pk_add_f32 v[60:61], v[64:65], v[132:133]
	v_pk_add_f32 v[62:63], v[70:71], v[146:147]
	v_pk_add_f32 v[64:65], v[72:73], v[148:149]
	v_pk_add_f32 v[66:67], v[74:75], v[162:163]
	v_pk_add_f32 v[68:69], v[76:77], v[164:165]
	v_pk_fma_f32 v[2:3], v[40:41], s[8:9], v[2:3] op_sel_hi:[1,0,1]
	v_pk_fma_f32 v[0:1], v[38:39], s[8:9], v[0:1] op_sel_hi:[1,0,1]
	s_mov_b32 s10, s5
	v_pk_fma_f32 v[6:7], v[44:45], s[8:9], v[6:7] op_sel_hi:[1,0,1]
	v_pk_fma_f32 v[4:5], v[42:43], s[8:9], v[4:5] op_sel_hi:[1,0,1]
	v_pk_fma_f32 v[10:11], v[48:49], s[8:9], v[10:11] op_sel_hi:[1,0,1]
	v_pk_fma_f32 v[8:9], v[46:47], s[8:9], v[8:9] op_sel_hi:[1,0,1]
	v_pk_fma_f32 v[14:15], v[52:53], s[8:9], v[14:15] op_sel_hi:[1,0,1]
	v_pk_fma_f32 v[12:13], v[50:51], s[8:9], v[12:13] op_sel_hi:[1,0,1]
	v_pk_fma_f32 v[18:19], v[56:57], s[8:9], v[18:19] op_sel_hi:[1,0,1]
	v_pk_fma_f32 v[16:17], v[54:55], s[8:9], v[16:17] op_sel_hi:[1,0,1]
	v_pk_fma_f32 v[22:23], v[60:61], s[8:9], v[22:23] op_sel_hi:[1,0,1]
	v_pk_fma_f32 v[20:21], v[58:59], s[8:9], v[20:21] op_sel_hi:[1,0,1]
	v_pk_fma_f32 v[26:27], v[64:65], s[8:9], v[26:27] op_sel_hi:[1,0,1]
	v_pk_fma_f32 v[24:25], v[62:63], s[8:9], v[24:25] op_sel_hi:[1,0,1]
	v_pk_fma_f32 v[30:31], v[68:69], s[8:9], v[30:31] op_sel_hi:[1,0,1]
	v_pk_fma_f32 v[28:29], v[66:67], s[8:9], v[28:29] op_sel_hi:[1,0,1]
	global_store_dwordx4 v[36:37], v[0:3], off offset:-4096
	global_store_dwordx4 v[36:37], v[4:7], off offset:-3072
	global_store_dwordx4 v[36:37], v[8:11], off offset:-2048
	global_store_dwordx4 v[36:37], v[12:15], off offset:-1024
	global_store_dwordx4 v[36:37], v[16:19], off
	global_store_dwordx4 v[36:37], v[20:23], off offset:1024
	global_store_dwordx4 v[36:37], v[24:27], off offset:2048
	global_store_dwordx4 v[36:37], v[28:31], off offset:3072
	v_lshl_add_u64 v[36:37], v[36:37], 0, s[6:7]
	s_cbranch_vccnz .LBB0_1225
